# speedup vs baseline: 1.0131x; 1.0131x over previous
.LBB3_16:
	s_or_b64 exec, exec, s[4:5]
	v_and_b32_e32 v92, 63, v0
	s_lshr_b32 s27, s26, 6
	v_lshlrev_b32_e32 v30, 2, v0
	v_mov_b32_e32 v31, -1
	v_mov_b32_e32 v34, 0
	v_cmp_gt_u32_e64 s[14:15], 12, v0
	s_and_saveexec_b64 s[16:17], s[14:15]
	ds_write_b32 v30, v31 offset:54144
	s_mov_b64 exec, s[16:17]
	s_waitcnt vmcnt(0)
	v_add_u32_e32 v42, v2, v3
	v_add_u32_e32 v52, v11, v5
	v_add_u32_e32 v43, v8, v42
	v_add_u32_e32 v53, v4, v52
	v_add_u32_e32 v44, v9, v43
	v_add_u32_e32 v54, v1, v53
	v_add_u32_e32 v45, v10, v44
	v_add_u32_e32 v55, v16, v54
	v_add_u32_e32 v46, v12, v45
	v_add_u32_e32 v56, v15, v55
	v_add_u32_e32 v47, v13, v46
	v_add_u32_e32 v57, v21, v56
	v_add_u32_e32 v48, v14, v47
	v_add_u32_e32 v58, v17, v57
	v_add_u32_e32 v49, 0x7f, v48
	v_add_u32_e32 v59, 0x7f, v58
	v_lshrrev_b32_e32 v49, 7, v49
	v_lshrrev_b32_e32 v59, 7, v59
	v_mov_b32_e32 v50, v49
	v_mov_b32_e32 v51, v59
	s_nop 0
	v_add_u32_dpp v50, v50, v50 row_shr:1 row_mask:0xf bank_mask:0xf
	v_add_u32_dpp v51, v51, v51 row_shr:1 row_mask:0xf bank_mask:0xf
	s_nop 0
	v_add_u32_dpp v50, v50, v50 row_shr:2 row_mask:0xf bank_mask:0xf
	v_add_u32_dpp v51, v51, v51 row_shr:2 row_mask:0xf bank_mask:0xf
	s_nop 0
	v_add_u32_dpp v50, v50, v50 row_shr:4 row_mask:0xf bank_mask:0xf
	v_add_u32_dpp v51, v51, v51 row_shr:4 row_mask:0xf bank_mask:0xf
	s_nop 0
	v_add_u32_dpp v50, v50, v50 row_shr:8 row_mask:0xf bank_mask:0xf
	v_add_u32_dpp v51, v51, v51 row_shr:8 row_mask:0xf bank_mask:0xf
	s_nop 0
	v_add_u32_dpp v50, v50, v50 row_bcast:15 row_mask:0xa bank_mask:0xf
	v_add_u32_dpp v51, v51, v51 row_bcast:15 row_mask:0xa bank_mask:0xf
	s_nop 0
	v_add_u32_dpp v50, v50, v50 row_bcast:31 row_mask:0xc bank_mask:0xf
	v_add_u32_dpp v51, v51, v51 row_bcast:31 row_mask:0xc bank_mask:0xf
	s_nop 0
	v_readlane_b32 s6, v50, 63
	s_lshl_b32 s7, s27, 2
	v_mov_b32_e32 v33, s7
	v_cmp_eq_u32_e64 s[14:15], 0, v92
	v_mov_b32_e32 v32, s6
	s_and_saveexec_b64 s[16:17], s[14:15]
	ds_write_b32 v33, v32 offset:54192
	s_mov_b64 exec, s[16:17]
	s_waitcnt lgkmcnt(0)
	s_barrier
	ds_read_b128 v[64:67], v34 offset:54192
	s_waitcnt lgkmcnt(0)
	v_readfirstlane_b32 s6, v64
	v_readfirstlane_b32 s7, v65
	v_readfirstlane_b32 s8, v66
	v_readfirstlane_b32 s9, v67
	s_nop 3
	s_add_u32 s10, s6, s7
	s_add_u32 s10, s10, s8
	s_add_u32 s10, s10, s9
	s_cmp_gt_u32 s27, 0
	s_cselect_b32 s14, s6, 0
	s_cmp_gt_u32 s27, 1
	s_cselect_b32 s15, s7, 0
	s_cmp_gt_u32 s27, 2
	s_cselect_b32 s16, s8, 0
	s_add_u32 s11, s14, s15
	s_add_u32 s11, s11, s16
	v_sub_u32_e32 v68, v50, v49
	v_sub_u32_e32 v69, v51, v59
	v_add_u32_e32 v68, s11, v68
	v_add_u32_e32 v69, s10, v69
	v_add_u32_e32 v70, v68, v49
	v_add_u32_e32 v71, v69, v59
	v_mov_b32_e32 v36, v0
	v_sub_u32_e32 v37, s2, v68
	v_mov_b32_e32 v38, v48
	v_mov_b32_e32 v39, v3
	v_or_b32_e32 v60, 0x100, v0
	v_sub_u32_e32 v61, s2, v69
	v_mov_b32_e32 v62, v58
	v_mov_b32_e32 v63, v5
	v_cmp_ge_u32_e64 s[14:15], s2, v68
	v_cmp_lt_u32_e64 s[16:17], s2, v70
	v_cmp_ge_u32_e64 s[6:7], s2, v69
	v_cmp_lt_u32_e64 s[8:9], s2, v71
	s_and_b64 s[14:15], s[14:15], s[16:17]
	s_and_b64 s[6:7], s[6:7], s[8:9]
	s_and_saveexec_b64 s[16:17], s[14:15]
	ds_write_b128 v34, v[36:39] offset:54144
	ds_write_b128 v34, v[42:45] offset:54160
	ds_write_b96 v34, v[46:48] offset:54176
	s_mov_b64 exec, s[16:17]
	s_and_saveexec_b64 s[16:17], s[6:7]
	ds_write_b128 v34, v[60:63] offset:54144
	ds_write_b128 v34, v[52:55] offset:54160
	ds_write_b96 v34, v[56:58] offset:54176
	s_mov_b64 exec, s[16:17]
	v_mov_b32_e32 v1, 0
	s_waitcnt lgkmcnt(0)
	s_barrier
	ds_read_b32 v2, v1 offset:54144
	s_waitcnt lgkmcnt(0)
	v_cmp_gt_i32_e32 vcc, 0, v2
	v_readfirstlane_b32 s2, v2
	s_cbranch_vccnz .LBB3_39
	v_mov_b32_e32 v5, 0xd39c
	s_load_dwordx2 s[22:23], s[0:1], 0x8
	s_load_dwordx2 s[18:19], s[0:1], 0x18
	v_mov_b32_e32 v2, 0xd384
	v_mov_b32_e32 v3, 0xd38c
	v_mov_b32_e32 v4, 0xd394
	ds_read2_b32 v[8:9], v5 offset1:1
	ds_read2_b32 v[6:7], v2 offset1:1
	ds_read2_b32 v[12:13], v3 offset1:1
	ds_read2_b32 v[10:11], v4 offset1:1
	ds_read_b32 v1, v1 offset:54180
	s_mov_b32 s28, 0
	s_cmp_lt_u32 s2, 23
	s_mov_b32 s0, s2
	s_cbranch_scc1 .LBB3_29
	s_movk_i32 s4, 0xffe8
	s_mov_b32 s1, 22
	s_mov_b32 s0, s2
